# MLA loop: max3 chain re-spaced across the PV gaps by issue-cost weight
# baseline (speedup 1.0000x reference)
; __device__ __forceinline__ void finishSM(f32x16& p0, f32x16& p1, float alpha, float& l_reg, bf16x8& pa0, bf16x8& pa1, bf16x8& pa2, bf16x8& pa3) {
; #pragma unroll
;     for (int r = 0; r < 16; ++r) p1[r] = EXP_PROBE ? fmaf(p1[r], 0.001f, 1.f) : __builtin_amdgcn_exp2f(p1[r]);
;     float ps = 0.f;
; #pragma unroll
;     for (int r = 0; r < 16; ++r) ps += p0[r];
; #pragma unroll
;     for (int r = 0; r < 16; ++r) ps += p1[r];
;     { auto rr = __builtin_amdgcn_permlane32_swap(__float_as_uint(ps), __float_as_uint(ps), false, false);
;       ps = __uint_as_float(rr[0]) + __uint_as_float(rr[1]); }
;     l_reg = l_reg * alpha + ps;
;     ATT_PKN(p0, 0, pa0); ATT_PKN(p0, 8, pa1); ATT_PKN(p1, 0, pa2); ATT_PKN(p1, 8, pa3);
; }
; template <int DQK> __device__ __forceinline__ void qkt(f32x16& p0, f32x16& p1, const LAS char* buf, const bf16x8* qr, int r32, int hi, const f32x16& negm) {
; #pragma unroll
;     for (int d0 = 0; d0 < 4; ++d0) { const int ch = d0 * 2 + hi;
;         const bf16x8 b0 = *(const LAS bf16x8*)(buf + B_KN + swz64(r32, ch));
;         const bf16x8 b1 = *(const LAS bf16x8*)(buf + B_KN + swz64(32 + r32, ch));
;         p0 = __builtin_amdgcn_mfma_f32_32x32x16_bf16(b0, qr[d0], d0 == 0 ? negm : p0, 0, 0, 0);
;         p1 = __builtin_amdgcn_mfma_f32_32x32x16_bf16(b1, qr[d0], d0 == 0 ? negm : p1, 0, 0, 0); }
;     if constexpr (DQK == 96) {
; #pragma unroll
;         for (int d0 = 0; d0 < 2; ++d0) { const int ch = d0 * 2 + hi;
;             const bf16x8 b0 = *(const LAS bf16x8*)(buf + B_KR + swz32(r32, ch));
;             const bf16x8 b1 = *(const LAS bf16x8*)(buf + B_KR + swz32(32 + r32, ch));
;             p0 = __builtin_amdgcn_mfma_f32_32x32x16_bf16(b0, qr[4 + d0], p0, 0, 0, 0);
;             p1 = __builtin_amdgcn_mfma_f32_32x32x16_bf16(b1, qr[4 + d0], p1, 0, 0, 0); }
;     }
; }
; template <int D0> __device__ __forceinline__ void pv_one(f32x16& od, unsigned vb, bf16x8 pa0, bf16x8 pa1, bf16x8 pa2, bf16x8 pa3) {
;     const s16x4 l0 = tr_read<v_rd_off(D0, 0, 0)>(vb), h0 = tr_read<v_rd_off(D0, 0, 1)>(vb), l1 = tr_read<v_rd_off(D0, 1, 0)>(vb), h1 = tr_read<v_rd_off(D0, 1, 1)>(vb);
;     const s16x4 l2 = tr_read<v_rd_off(D0, 2, 0)>(vb), h2 = tr_read<v_rd_off(D0, 2, 1)>(vb), l3 = tr_read<v_rd_off(D0, 3, 0)>(vb), h3 = tr_read<v_rd_off(D0, 3, 1)>(vb);
;     asm volatile("s_waitcnt lgkmcnt(0)" ::: "memory"); SBAR();
.LBB0_523:
	s_waitcnt lgkmcnt(0)
	s_barrier
	ds_read_b128 v[4:7], v209 offset:20480
	ds_read_b128 v[8:11], v209 offset:24576
	ds_read_b128 v[174:177], v210 offset:20480
	ds_read_b128 v[246:249], v210 offset:24576
	ds_read_b128 v[250:253], v211 offset:20480
	ds_read_b128 v[78:81], v211 offset:24576
	ds_read_b128 v[12:15], v212 offset:20480
	v_exp_f32_e32 v98, v98
	v_exp_f32_e32 v99, v99
	v_exp_f32_e32 v100, v100
	v_exp_f32_e32 v101, v101
	v_exp_f32_e32 v102, v102
	v_exp_f32_e32 v103, v103
	v_exp_f32_e32 v104, v104
	v_exp_f32_e32 v105, v105
	s_waitcnt lgkmcnt(6)
	v_mfma_f32_32x32x16_bf16 v[130:145], v[4:7], v[166:169], v[82:97]
	ds_read_b128 v[4:7], v212 offset:24576
	v_exp_f32_e32 v106, v106
	v_exp_f32_e32 v107, v107
	v_exp_f32_e32 v108, v108
	v_cvt_pk_bf16_f32 v74, v243, v245
	s_waitcnt lgkmcnt(6)
	v_mfma_f32_32x32x16_bf16 v[114:129], v[8:11], v[166:169], v[82:97]
	ds_read_b128 v[8:11], v219 offset:28672
	v_exp_f32_e32 v109, v109
	v_exp_f32_e32 v110, v110
	v_exp_f32_e32 v111, v111
	v_cvt_pk_bf16_f32 v75, v241, v244
	s_waitcnt lgkmcnt(6)
	v_mfma_f32_32x32x16_bf16 v[130:145], v[174:177], v[162:165], v[130:145]
	ds_read_b128 v[174:177], v219 offset:30720
	v_exp_f32_e32 v112, v112
	v_exp_f32_e32 v113, v113
	v_cvt_pk_bf16_f32 v76, v239, v242
	v_cvt_pk_bf16_f32 v77, v238, v240
	v_add_f32_e32 v229, v243, v245
	v_add_f32_e32 v229, v241, v229
	s_waitcnt lgkmcnt(6)
	v_mfma_f32_32x32x16_bf16 v[114:129], v[246:249], v[162:165], v[114:129]
	ds_read_b128 v[246:249], v220 offset:28672
	v_cvt_pk_bf16_f32 v66, v236, v237
	v_cvt_pk_bf16_f32 v67, v233, v235
	v_add_f32_e32 v229, v244, v229
	v_add_f32_e32 v229, v239, v229
	v_add_f32_e32 v229, v242, v229
	v_add_f32_e32 v229, v238, v229
	s_waitcnt lgkmcnt(6)
	v_mfma_f32_32x32x16_bf16 v[130:145], v[250:253], v[158:161], v[130:145]
	ds_read_b128 v[250:253], v220 offset:30720
	v_cvt_pk_bf16_f32 v68, v231, v234
	v_cvt_pk_bf16_f32 v69, v230, v232
	v_add_f32_e32 v229, v240, v229
	v_add_f32_e32 v229, v236, v229
	v_add_f32_e32 v229, v237, v229
	v_add_f32_e32 v229, v233, v229
	s_waitcnt lgkmcnt(6)
	v_mfma_f32_32x32x16_bf16 v[114:129], v[78:81], v[158:161], v[114:129]
	v_add_f32_e32 v229, v235, v229
	v_add_f32_e32 v229, v231, v229
	v_add_f32_e32 v229, v234, v229
	v_add_f32_e32 v229, v230, v229
	v_add_f32_e32 v229, v232, v229
	v_add_f32_e32 v229, v98, v229
	s_waitcnt lgkmcnt(5)
	v_mfma_f32_32x32x16_bf16 v[130:145], v[12:15], v[154:157], v[130:145]
	ds_read_b64_tr_b16 v[230:231], v213 offset:0
	ds_read_b64_tr_b16 v[232:233], v213 offset:1024
	ds_read_b64_tr_b16 v[234:235], v213 offset:2048
	ds_read_b64_tr_b16 v[236:237], v213 offset:3072
	v_add_f32_e32 v229, v99, v229
	v_add_f32_e32 v229, v100, v229
	v_add_f32_e32 v229, v101, v229
	s_waitcnt lgkmcnt(8)
	v_mfma_f32_32x32x16_bf16 v[114:129], v[4:7], v[154:157], v[114:129]
	ds_read_b64_tr_b16 v[238:239], v213 offset:4096
	ds_read_b64_tr_b16 v[240:241], v213 offset:5120
	ds_read_b64_tr_b16 v[242:243], v213 offset:6144
	ds_read_b64_tr_b16 v[244:245], v213 offset:7168
	v_add_f32_e32 v229, v102, v229
	v_add_f32_e32 v229, v103, v229
	v_add_f32_e32 v229, v104, v229
	s_waitcnt lgkmcnt(11)
	v_mfma_f32_32x32x16_bf16 v[130:145], v[8:11], v[150:153], v[130:145]
	v_add_f32_e32 v229, v105, v229
	v_add_f32_e32 v229, v106, v229
	v_add_f32_e32 v229, v107, v229
	v_add_f32_e32 v229, v108, v229
	v_add_f32_e32 v229, v109, v229
	v_add_f32_e32 v229, v110, v229
	s_waitcnt lgkmcnt(10)
	v_mfma_f32_32x32x16_bf16 v[114:129], v[174:177], v[150:153], v[114:129]
	v_add_f32_e32 v229, v111, v229
	v_add_f32_e32 v229, v112, v229
	v_add_f32_e32 v228, v113, v229
	s_add_i32 s36, s35, -1
	s_cmp_lt_u32 s36, s30
	s_cselect_b32 s0, 0, s30
	s_cselect_b32 s1, s29, s34
	s_lshl_b32 s0, s0, 6
	s_sub_i32 s37, s1, s0
	s_lshl_b32 s1, s36, 6
	s_add_i32 s37, s37, s1
	s_lshl_b32 s0, s37, 6
	s_add_u32 s48, s44, s0
	s_addc_u32 s49, s45, 0
	s_lshl_b32 s0, s37, 11
	s_add_u32 s46, s42, s0
	s_addc_u32 s47, s43, 0
	global_load_dwordx4 v[174:177], v226, s[48:49]
	s_waitcnt lgkmcnt(9)
	v_mfma_f32_32x32x16_bf16 v[130:145], v[246:249], v[146:149], v[130:145]
	v_cvt_pk_bf16_f32 v70, v98, v99
	v_cvt_pk_bf16_f32 v71, v100, v101
	v_cvt_pk_bf16_f32 v72, v102, v103
	v_cvt_pk_bf16_f32 v73, v104, v105
	global_load_dwordx4 v[8:11], v225, s[46:47]
	global_load_dwordx4 v[4:7], v225, s[46:47] offset:128
	s_waitcnt lgkmcnt(8)
	v_mfma_f32_32x32x16_bf16 v[114:129], v[250:253], v[146:149], v[114:129]
	v_cvt_pk_bf16_f32 v12, v106, v107
	v_cvt_pk_bf16_f32 v13, v108, v109
	v_cvt_pk_bf16_f32 v14, v110, v111
	v_cvt_pk_bf16_f32 v15, v112, v113
	ds_read_b64_tr_b16 v[78:79], v213 offset:512
	ds_read_b64_tr_b16 v[80:81], v213 offset:1536
	ds_read_b64_tr_b16 v[98:99], v213 offset:2560
	ds_read_b64_tr_b16 v[100:101], v213 offset:3584
	ds_read_b64_tr_b16 v[102:103], v213 offset:4608
	ds_read_b64_tr_b16 v[104:105], v213 offset:5632
	ds_read_b64_tr_b16 v[110:111], v213 offset:6656
	ds_read_b64_tr_b16 v[112:113], v213 offset:7680
	v_max3_f32 v2, v130, v131, v132
	v_max3_f32 v2, v2, v133, v134
	v_max3_f32 v2, v2, v135, v136
	v_max3_f32 v2, v2, v137, v138
	v_max3_f32 v2, v2, v139, v140
	v_max3_f32 v2, v2, v141, v142
	s_waitcnt lgkmcnt(8)
	v_mfma_f32_32x32x16_bf16 v[50:65], v[230:233], v[74:77], v[50:65]
	v_max3_f32 v2, v2, v143, v144
	v_max3_f32 v2, v2, v145, v114
	v_max3_f32 v2, v2, v115, v116
	v_max3_f32 v2, v2, v117, v118
	v_mfma_f32_32x32x16_bf16 v[50:65], v[234:237], v[66:69], v[50:65]
	v_max3_f32 v2, v2, v119, v120
	v_max3_f32 v2, v2, v121, v122
	v_max3_f32 v2, v2, v123, v124
	v_mfma_f32_32x32x16_bf16 v[50:65], v[238:241], v[70:73], v[50:65]
	v_max3_f32 v2, v2, v125, v126
	v_max3_f32 v2, v2, v127, v128
	v_max_f32_e32 v2, v2, v129
	v_mfma_f32_32x32x16_bf16 v[50:65], v[242:245], v[12:15], v[50:65]
	v_cmp_ge_f32_e32 vcc, s28, v2
	s_cmp_eq_u64 vcc, exec
	s_cbranch_scc0 .LBB0_542_0
	v_mov_b32_e32 v2, 1.0

; #define SBAR() __builtin_amdgcn_sched_barrier(0)
; __device__ __forceinline__ float psm_max(const f32x16& p0, const f32x16& p1) {
;     float pmax = p0[0];
; #pragma unroll
;     for (int r = 1; r < 16; ++r) pmax = fmaxf(pmax, p0[r]);
; #pragma unroll
;     for (int r = 0; r < 16; ++r) pmax = fmaxf(pmax, p1[r]);
;     { auto rr = __builtin_amdgcn_permlane32_swap(__float_as_uint(pmax), __float_as_uint(pmax), false, false);
;       pmax = fmaxf(__uint_as_float(rr[0]), __uint_as_float(rr[1])); }
;     return pmax;
; }
; template <int D0> __device__ __forceinline__ void pv_one(f32x16& od, unsigned vb, bf16x8 pa0, bf16x8 pa1, bf16x8 pa2, bf16x8 pa3) {
;     const s16x4 l0 = tr_read<v_rd_off(D0, 0, 0)>(vb), h0 = tr_read<v_rd_off(D0, 0, 1)>(vb), l1 = tr_read<v_rd_off(D0, 1, 0)>(vb), h1 = tr_read<v_rd_off(D0, 1, 1)>(vb);
;     const s16x4 l2 = tr_read<v_rd_off(D0, 2, 0)>(vb), h2 = tr_read<v_rd_off(D0, 2, 1)>(vb), l3 = tr_read<v_rd_off(D0, 3, 0)>(vb), h3 = tr_read<v_rd_off(D0, 3, 1)>(vb);
;     asm volatile("s_waitcnt lgkmcnt(0)" ::: "memory"); SBAR();
;     ...
;     od = __builtin_amdgcn_mfma_f32_32x32x16_bf16(ATT_PK(l0, h0), pa0, od, 0, 0, 0);
;     od = __builtin_amdgcn_mfma_f32_32x32x16_bf16(ATT_PK(l1, h1), pa1, od, 0, 0, 0);
;     od = __builtin_amdgcn_mfma_f32_32x32x16_bf16(ATT_PK(l2, h2), pa2, od, 0, 0, 0);
;     od = __builtin_amdgcn_mfma_f32_32x32x16_bf16(ATT_PK(l3, h3), pa3, od, 0, 0, 0);
;     ...
; }
.Lmla_b_ld_done_0:
	s_waitcnt lgkmcnt(8)
	v_mfma_f32_32x32x16_bf16 v[98:113], v[70:73], v[146:149], v[98:113]
	v_cvt_pk_bf16_f32 v118, v122, v123
	v_cvt_pk_bf16_f32 v119, v124, v125
	v_cvt_pk_bf16_f32 v120, v126, v127
	v_cvt_pk_bf16_f32 v121, v128, v129
	v_add_f32_e32 v126, v129, v252
	ds_read_b64_tr_b16 v[66:67], v213 offset:20992
	ds_read_b64_tr_b16 v[68:69], v213 offset:22016
	ds_read_b64_tr_b16 v[70:71], v213 offset:23040
	ds_read_b64_tr_b16 v[72:73], v213 offset:24064
	ds_read_b64_tr_b16 v[74:75], v213 offset:25088
	ds_read_b64_tr_b16 v[76:77], v213 offset:26112
	ds_read_b64_tr_b16 v[78:79], v213 offset:27136
	ds_read_b64_tr_b16 v[80:81], v213 offset:28160
	v_max3_f32 v250, v130, v131, v132
	v_max3_f32 v250, v250, v133, v134
	v_max3_f32 v250, v250, v135, v136
	v_max3_f32 v250, v250, v137, v138
	v_max3_f32 v250, v250, v139, v140
	v_max3_f32 v250, v250, v141, v142
	s_waitcnt lgkmcnt(8)
	v_mfma_f32_32x32x16_bf16 v[50:65], v[234:237], v[12:15], v[50:65]
	v_max3_f32 v250, v250, v143, v144
	v_max3_f32 v250, v250, v145, v98
	v_max3_f32 v250, v250, v99, v100
	v_max3_f32 v250, v250, v101, v102
	v_mfma_f32_32x32x16_bf16 v[50:65], v[238:241], v[230:233], v[50:65]
	v_max3_f32 v250, v250, v103, v104
	v_max3_f32 v250, v250, v105, v106
	v_max3_f32 v250, v250, v107, v108
	v_mfma_f32_32x32x16_bf16 v[50:65], v[242:245], v[114:117], v[50:65]
	v_max3_f32 v250, v250, v109, v110
	v_max3_f32 v250, v250, v111, v112
	v_max_f32_e32 v250, v250, v113
	v_mfma_f32_32x32x16_bf16 v[50:65], v[246:249], v[118:121], v[50:65]
	v_cmp_ge_f32_e32 vcc, s28, v250
	s_cmp_eq_u64 vcc, exec
	v_mov_b32_e32 v16, 1.0
	s_cbranch_scc0 .LBB0_543_0

; __device__ __forceinline__ void finishSM(f32x16& p0, f32x16& p1, float alpha, float& l_reg, bf16x8& pa0, bf16x8& pa1, bf16x8& pa2, bf16x8& pa3) {
; #pragma unroll
;     for (int r = 0; r < 16; ++r) p1[r] = EXP_PROBE ? fmaf(p1[r], 0.001f, 1.f) : __builtin_amdgcn_exp2f(p1[r]);
;     float ps = 0.f;
; #pragma unroll
;     for (int r = 0; r < 16; ++r) ps += p0[r];
; #pragma unroll
;     for (int r = 0; r < 16; ++r) ps += p1[r];
;     { auto rr = __builtin_amdgcn_permlane32_swap(__float_as_uint(ps), __float_as_uint(ps), false, false);
;       ps = __uint_as_float(rr[0]) + __uint_as_float(rr[1]); }
;     l_reg = l_reg * alpha + ps;
;     ATT_PKN(p0, 0, pa0); ATT_PKN(p0, 8, pa1); ATT_PKN(p1, 0, pa2); ATT_PKN(p1, 8, pa3);
; }
; template <int DQK> __device__ __forceinline__ void qkt(f32x16& p0, f32x16& p1, const LAS char* buf, const bf16x8* qr, int r32, int hi, const f32x16& negm) {
; #pragma unroll
;     for (int d0 = 0; d0 < 4; ++d0) { const int ch = d0 * 2 + hi;
;         const bf16x8 b0 = *(const LAS bf16x8*)(buf + B_KN + swz64(r32, ch));
;         const bf16x8 b1 = *(const LAS bf16x8*)(buf + B_KN + swz64(32 + r32, ch));
;         p0 = __builtin_amdgcn_mfma_f32_32x32x16_bf16(b0, qr[d0], d0 == 0 ? negm : p0, 0, 0, 0);
;         p1 = __builtin_amdgcn_mfma_f32_32x32x16_bf16(b1, qr[d0], d0 == 0 ? negm : p1, 0, 0, 0); }
;     if constexpr (DQK == 96) {
; #pragma unroll
;         for (int d0 = 0; d0 < 2; ++d0) { const int ch = d0 * 2 + hi;
;             const bf16x8 b0 = *(const LAS bf16x8*)(buf + B_KR + swz32(r32, ch));
;             const bf16x8 b1 = *(const LAS bf16x8*)(buf + B_KR + swz32(32 + r32, ch));
;             p0 = __builtin_amdgcn_mfma_f32_32x32x16_bf16(b0, qr[4 + d0], p0, 0, 0, 0);
;             p1 = __builtin_amdgcn_mfma_f32_32x32x16_bf16(b1, qr[4 + d0], p1, 0, 0, 0); }
;     }
; }
; template <int D0> __device__ __forceinline__ void pv_one(f32x16& od, unsigned vb, bf16x8 pa0, bf16x8 pa1, bf16x8 pa2, bf16x8 pa3) {
;     const s16x4 l0 = tr_read<v_rd_off(D0, 0, 0)>(vb), h0 = tr_read<v_rd_off(D0, 0, 1)>(vb), l1 = tr_read<v_rd_off(D0, 1, 0)>(vb), h1 = tr_read<v_rd_off(D0, 1, 1)>(vb);
;     const s16x4 l2 = tr_read<v_rd_off(D0, 2, 0)>(vb), h2 = tr_read<v_rd_off(D0, 2, 1)>(vb), l3 = tr_read<v_rd_off(D0, 3, 0)>(vb), h3 = tr_read<v_rd_off(D0, 3, 1)>(vb);
;     asm volatile("s_waitcnt lgkmcnt(0)" ::: "memory"); SBAR();
.LBB0_540_0:
	v_fmac_f32_e32 v228, v227, v223
	s_add_i32 s35, s35, 2
	v_fma_f32 v223, v228, v2, v126
	s_cmp_ge_u32 s36, s12
	s_cbranch_scc1 .Lmla_exit_0
	v_mov_b32_e32 v227, v16
	s_waitcnt lgkmcnt(0)
	s_barrier
	ds_read_b128 v[4:7], v209 offset:0
	ds_read_b128 v[8:11], v209 offset:4096
	ds_read_b128 v[174:177], v210 offset:0
	ds_read_b128 v[246:249], v210 offset:4096
	ds_read_b128 v[250:253], v211 offset:0
	ds_read_b128 v[78:81], v211 offset:4096
	ds_read_b128 v[12:15], v212 offset:0
	v_exp_f32_e32 v98, v98
	v_exp_f32_e32 v99, v99
	v_exp_f32_e32 v100, v100
	v_exp_f32_e32 v101, v101
	v_exp_f32_e32 v102, v102
	v_exp_f32_e32 v103, v103
	v_exp_f32_e32 v104, v104
	v_exp_f32_e32 v105, v105
	s_waitcnt lgkmcnt(6)
	v_mfma_f32_32x32x16_bf16 v[130:145], v[4:7], v[166:169], v[82:97]
	ds_read_b128 v[4:7], v212 offset:4096
	v_exp_f32_e32 v106, v106
	v_exp_f32_e32 v107, v107
	v_exp_f32_e32 v108, v108
	v_cvt_pk_bf16_f32 v74, v243, v245
	s_waitcnt lgkmcnt(6)
	v_mfma_f32_32x32x16_bf16 v[114:129], v[8:11], v[166:169], v[82:97]
	ds_read_b128 v[8:11], v219 offset:8192
	v_exp_f32_e32 v109, v109
	v_exp_f32_e32 v110, v110
	v_exp_f32_e32 v111, v111
	v_cvt_pk_bf16_f32 v75, v241, v244
	s_waitcnt lgkmcnt(6)
	v_mfma_f32_32x32x16_bf16 v[130:145], v[174:177], v[162:165], v[130:145]
	ds_read_b128 v[174:177], v219 offset:10240
	v_exp_f32_e32 v112, v112
	v_exp_f32_e32 v113, v113
	v_cvt_pk_bf16_f32 v76, v239, v242
	v_cvt_pk_bf16_f32 v77, v238, v240
	v_add_f32_e32 v229, v243, v245
	v_add_f32_e32 v229, v241, v229
	s_waitcnt lgkmcnt(6)
	v_mfma_f32_32x32x16_bf16 v[114:129], v[246:249], v[162:165], v[114:129]
	ds_read_b128 v[246:249], v220 offset:8192
	v_cvt_pk_bf16_f32 v66, v236, v237
	v_cvt_pk_bf16_f32 v67, v233, v235
	v_add_f32_e32 v229, v244, v229
	v_add_f32_e32 v229, v239, v229
	v_add_f32_e32 v229, v242, v229
	v_add_f32_e32 v229, v238, v229
	s_waitcnt lgkmcnt(6)
	v_mfma_f32_32x32x16_bf16 v[130:145], v[250:253], v[158:161], v[130:145]
	ds_read_b128 v[250:253], v220 offset:10240
	v_cvt_pk_bf16_f32 v68, v231, v234
	v_cvt_pk_bf16_f32 v69, v230, v232
	v_add_f32_e32 v229, v240, v229
	v_add_f32_e32 v229, v236, v229
	v_add_f32_e32 v229, v237, v229
	v_add_f32_e32 v229, v233, v229
	s_waitcnt lgkmcnt(6)
	v_mfma_f32_32x32x16_bf16 v[114:129], v[78:81], v[158:161], v[114:129]
	v_add_f32_e32 v229, v235, v229
	v_add_f32_e32 v229, v231, v229
	v_add_f32_e32 v229, v234, v229
	v_add_f32_e32 v229, v230, v229
	v_add_f32_e32 v229, v232, v229
	v_add_f32_e32 v229, v98, v229
	s_waitcnt lgkmcnt(5)
	v_mfma_f32_32x32x16_bf16 v[130:145], v[12:15], v[154:157], v[130:145]
	ds_read_b64_tr_b16 v[230:231], v213 offset:40960
	ds_read_b64_tr_b16 v[232:233], v213 offset:41984
	ds_read_b64_tr_b16 v[234:235], v213 offset:43008
	ds_read_b64_tr_b16 v[236:237], v213 offset:44032
	v_add_f32_e32 v229, v99, v229
	v_add_f32_e32 v229, v100, v229
	v_add_f32_e32 v229, v101, v229
	s_waitcnt lgkmcnt(8)
	v_mfma_f32_32x32x16_bf16 v[114:129], v[4:7], v[154:157], v[114:129]
	ds_read_b64_tr_b16 v[238:239], v213 offset:45056
	ds_read_b64_tr_b16 v[240:241], v213 offset:46080
	ds_read_b64_tr_b16 v[242:243], v213 offset:47104
	ds_read_b64_tr_b16 v[244:245], v213 offset:48128
	v_add_f32_e32 v229, v102, v229
	v_add_f32_e32 v229, v103, v229
	v_add_f32_e32 v229, v104, v229
	s_waitcnt lgkmcnt(11)
	v_mfma_f32_32x32x16_bf16 v[130:145], v[8:11], v[150:153], v[130:145]
	v_add_f32_e32 v229, v105, v229
	v_add_f32_e32 v229, v106, v229
	v_add_f32_e32 v229, v107, v229
	v_add_f32_e32 v229, v108, v229
	v_add_f32_e32 v229, v109, v229
	v_add_f32_e32 v229, v110, v229
	s_waitcnt lgkmcnt(10)
	v_mfma_f32_32x32x16_bf16 v[114:129], v[174:177], v[150:153], v[114:129]
	v_add_f32_e32 v229, v111, v229
	v_add_f32_e32 v229, v112, v229
	v_add_f32_e32 v228, v113, v229
	s_add_i32 s36, s35, -1
	s_cmp_lt_u32 s36, s30
	s_cselect_b32 s0, 0, s30
	s_cselect_b32 s1, s29, s34
	s_lshl_b32 s0, s0, 6
	s_sub_i32 s37, s1, s0
	s_lshl_b32 s1, s36, 6
	s_add_i32 s37, s37, s1
	s_lshl_b32 s0, s37, 6
	s_add_u32 s48, s44, s0
	s_addc_u32 s49, s45, 0
	s_lshl_b32 s0, s37, 11
	s_add_u32 s46, s42, s0
	s_addc_u32 s47, s43, 0
	global_load_dwordx4 v[174:177], v226, s[48:49]
	s_waitcnt lgkmcnt(9)
	v_mfma_f32_32x32x16_bf16 v[130:145], v[246:249], v[146:149], v[130:145]
	v_cvt_pk_bf16_f32 v70, v98, v99
	v_cvt_pk_bf16_f32 v71, v100, v101
	v_cvt_pk_bf16_f32 v72, v102, v103
	v_cvt_pk_bf16_f32 v73, v104, v105
	global_load_dwordx4 v[8:11], v225, s[46:47]
	global_load_dwordx4 v[4:7], v225, s[46:47] offset:128
	s_waitcnt lgkmcnt(8)
	v_mfma_f32_32x32x16_bf16 v[114:129], v[250:253], v[146:149], v[114:129]
	v_cvt_pk_bf16_f32 v12, v106, v107
	v_cvt_pk_bf16_f32 v13, v108, v109
	v_cvt_pk_bf16_f32 v14, v110, v111
	v_cvt_pk_bf16_f32 v15, v112, v113
	ds_read_b64_tr_b16 v[78:79], v213 offset:41472
	ds_read_b64_tr_b16 v[80:81], v213 offset:42496
	ds_read_b64_tr_b16 v[98:99], v213 offset:43520
	ds_read_b64_tr_b16 v[100:101], v213 offset:44544
	ds_read_b64_tr_b16 v[102:103], v213 offset:45568
	ds_read_b64_tr_b16 v[104:105], v213 offset:46592
	ds_read_b64_tr_b16 v[110:111], v213 offset:47616
	ds_read_b64_tr_b16 v[112:113], v213 offset:48640
	v_max3_f32 v2, v130, v131, v132
	v_max3_f32 v2, v2, v133, v134
	v_max3_f32 v2, v2, v135, v136
	v_max3_f32 v2, v2, v137, v138
	v_max3_f32 v2, v2, v139, v140
	v_max3_f32 v2, v2, v141, v142
	s_waitcnt lgkmcnt(8)
	v_mfma_f32_32x32x16_bf16 v[50:65], v[230:233], v[74:77], v[50:65]
	v_max3_f32 v2, v2, v143, v144
	v_max3_f32 v2, v2, v145, v114
	v_max3_f32 v2, v2, v115, v116
	v_max3_f32 v2, v2, v117, v118
	v_mfma_f32_32x32x16_bf16 v[50:65], v[234:237], v[66:69], v[50:65]
	v_max3_f32 v2, v2, v119, v120
	v_max3_f32 v2, v2, v121, v122
	v_max3_f32 v2, v2, v123, v124
	v_mfma_f32_32x32x16_bf16 v[50:65], v[238:241], v[70:73], v[50:65]
	v_max3_f32 v2, v2, v125, v126
	v_max3_f32 v2, v2, v127, v128
	v_max_f32_e32 v2, v2, v129
	v_mfma_f32_32x32x16_bf16 v[50:65], v[242:245], v[12:15], v[50:65]
	v_cmp_ge_f32_e32 vcc, s28, v2
	s_cmp_eq_u64 vcc, exec
	s_cbranch_scc0 .LBB0_542_1
	v_mov_b32_e32 v2, 1.0

; #define SBAR() __builtin_amdgcn_sched_barrier(0)
; __device__ __forceinline__ float psm_max(const f32x16& p0, const f32x16& p1) {
;     float pmax = p0[0];
; #pragma unroll
;     for (int r = 1; r < 16; ++r) pmax = fmaxf(pmax, p0[r]);
; #pragma unroll
;     for (int r = 0; r < 16; ++r) pmax = fmaxf(pmax, p1[r]);
;     { auto rr = __builtin_amdgcn_permlane32_swap(__float_as_uint(pmax), __float_as_uint(pmax), false, false);
;       pmax = fmaxf(__uint_as_float(rr[0]), __uint_as_float(rr[1])); }
;     return pmax;
; }
; template <int D0> __device__ __forceinline__ void pv_one(f32x16& od, unsigned vb, bf16x8 pa0, bf16x8 pa1, bf16x8 pa2, bf16x8 pa3) {
;     const s16x4 l0 = tr_read<v_rd_off(D0, 0, 0)>(vb), h0 = tr_read<v_rd_off(D0, 0, 1)>(vb), l1 = tr_read<v_rd_off(D0, 1, 0)>(vb), h1 = tr_read<v_rd_off(D0, 1, 1)>(vb);
;     const s16x4 l2 = tr_read<v_rd_off(D0, 2, 0)>(vb), h2 = tr_read<v_rd_off(D0, 2, 1)>(vb), l3 = tr_read<v_rd_off(D0, 3, 0)>(vb), h3 = tr_read<v_rd_off(D0, 3, 1)>(vb);
;     asm volatile("s_waitcnt lgkmcnt(0)" ::: "memory"); SBAR();
;     ...
;     od = __builtin_amdgcn_mfma_f32_32x32x16_bf16(ATT_PK(l0, h0), pa0, od, 0, 0, 0);
;     od = __builtin_amdgcn_mfma_f32_32x32x16_bf16(ATT_PK(l1, h1), pa1, od, 0, 0, 0);
;     od = __builtin_amdgcn_mfma_f32_32x32x16_bf16(ATT_PK(l2, h2), pa2, od, 0, 0, 0);
;     od = __builtin_amdgcn_mfma_f32_32x32x16_bf16(ATT_PK(l3, h3), pa3, od, 0, 0, 0);
;     ...
; }
.Lmla_b_ld_done_1:
	s_waitcnt lgkmcnt(8)
	v_mfma_f32_32x32x16_bf16 v[98:113], v[70:73], v[146:149], v[98:113]
	v_cvt_pk_bf16_f32 v118, v122, v123
	v_cvt_pk_bf16_f32 v119, v124, v125
	v_cvt_pk_bf16_f32 v120, v126, v127
	v_cvt_pk_bf16_f32 v121, v128, v129
	v_add_f32_e32 v126, v129, v252
	ds_read_b64_tr_b16 v[66:67], v213 offset:512
	ds_read_b64_tr_b16 v[68:69], v213 offset:1536
	ds_read_b64_tr_b16 v[70:71], v213 offset:2560
	ds_read_b64_tr_b16 v[72:73], v213 offset:3584
	ds_read_b64_tr_b16 v[74:75], v213 offset:4608
	ds_read_b64_tr_b16 v[76:77], v213 offset:5632
	ds_read_b64_tr_b16 v[78:79], v213 offset:6656
	ds_read_b64_tr_b16 v[80:81], v213 offset:7680
	v_max3_f32 v250, v130, v131, v132
	v_max3_f32 v250, v250, v133, v134
	v_max3_f32 v250, v250, v135, v136
	v_max3_f32 v250, v250, v137, v138
	v_max3_f32 v250, v250, v139, v140
	v_max3_f32 v250, v250, v141, v142
	s_waitcnt lgkmcnt(8)
	v_mfma_f32_32x32x16_bf16 v[50:65], v[234:237], v[12:15], v[50:65]
	v_max3_f32 v250, v250, v143, v144
	v_max3_f32 v250, v250, v145, v98
	v_max3_f32 v250, v250, v99, v100
	v_max3_f32 v250, v250, v101, v102
	v_mfma_f32_32x32x16_bf16 v[50:65], v[238:241], v[230:233], v[50:65]
	v_max3_f32 v250, v250, v103, v104
	v_max3_f32 v250, v250, v105, v106
	v_max3_f32 v250, v250, v107, v108
	v_mfma_f32_32x32x16_bf16 v[50:65], v[242:245], v[114:117], v[50:65]
	v_max3_f32 v250, v250, v109, v110
	v_max3_f32 v250, v250, v111, v112
	v_max_f32_e32 v250, v250, v113
	v_mfma_f32_32x32x16_bf16 v[50:65], v[246:249], v[118:121], v[50:65]
	v_cmp_ge_f32_e32 vcc, s28, v250
	s_cmp_eq_u64 vcc, exec
	v_mov_b32_e32 v16, 1.0
	s_cbranch_scc0 .LBB0_543_1

; __device__ __forceinline__ void finishSM(f32x16& p0, f32x16& p1, float alpha, float& l_reg, bf16x8& pa0, bf16x8& pa1, bf16x8& pa2, bf16x8& pa3) {
; #pragma unroll
;     for (int r = 0; r < 16; ++r) p1[r] = EXP_PROBE ? fmaf(p1[r], 0.001f, 1.f) : __builtin_amdgcn_exp2f(p1[r]);
;     float ps = 0.f;
; #pragma unroll
;     for (int r = 0; r < 16; ++r) ps += p0[r];
; #pragma unroll
;     for (int r = 0; r < 16; ++r) ps += p1[r];
;     { auto rr = __builtin_amdgcn_permlane32_swap(__float_as_uint(ps), __float_as_uint(ps), false, false);
;       ps = __uint_as_float(rr[0]) + __uint_as_float(rr[1]); }
;     l_reg = l_reg * alpha + ps;
;     ATT_PKN(p0, 0, pa0); ATT_PKN(p0, 8, pa1); ATT_PKN(p1, 0, pa2); ATT_PKN(p1, 8, pa3);
; }
; template <int DQK> __device__ __forceinline__ void qkt(f32x16& p0, f32x16& p1, const LAS char* buf, const bf16x8* qr, int r32, int hi, const f32x16& negm) {
; #pragma unroll
;     for (int d0 = 0; d0 < 4; ++d0) { const int ch = d0 * 2 + hi;
;         const bf16x8 b0 = *(const LAS bf16x8*)(buf + B_KN + swz64(r32, ch));
;         const bf16x8 b1 = *(const LAS bf16x8*)(buf + B_KN + swz64(32 + r32, ch));
;         p0 = __builtin_amdgcn_mfma_f32_32x32x16_bf16(b0, qr[d0], d0 == 0 ? negm : p0, 0, 0, 0);
;         p1 = __builtin_amdgcn_mfma_f32_32x32x16_bf16(b1, qr[d0], d0 == 0 ? negm : p1, 0, 0, 0); }
;     if constexpr (DQK == 96) {
; #pragma unroll
;         for (int d0 = 0; d0 < 2; ++d0) { const int ch = d0 * 2 + hi;
;             const bf16x8 b0 = *(const LAS bf16x8*)(buf + B_KR + swz32(r32, ch));
;             const bf16x8 b1 = *(const LAS bf16x8*)(buf + B_KR + swz32(32 + r32, ch));
;             p0 = __builtin_amdgcn_mfma_f32_32x32x16_bf16(b0, qr[4 + d0], p0, 0, 0, 0);
;             p1 = __builtin_amdgcn_mfma_f32_32x32x16_bf16(b1, qr[4 + d0], p1, 0, 0, 0); }
;     }
; }
; template <int D0> __device__ __forceinline__ void pv_one(f32x16& od, unsigned vb, bf16x8 pa0, bf16x8 pa1, bf16x8 pa2, bf16x8 pa3) {
;     const s16x4 l0 = tr_read<v_rd_off(D0, 0, 0)>(vb), h0 = tr_read<v_rd_off(D0, 0, 1)>(vb), l1 = tr_read<v_rd_off(D0, 1, 0)>(vb), h1 = tr_read<v_rd_off(D0, 1, 1)>(vb);
;     const s16x4 l2 = tr_read<v_rd_off(D0, 2, 0)>(vb), h2 = tr_read<v_rd_off(D0, 2, 1)>(vb), l3 = tr_read<v_rd_off(D0, 3, 0)>(vb), h3 = tr_read<v_rd_off(D0, 3, 1)>(vb);
;     asm volatile("s_waitcnt lgkmcnt(0)" ::: "memory"); SBAR();
.LBB0_540_1:
	v_fmac_f32_e32 v228, v227, v223
	s_add_i32 s35, s35, 2
	v_fma_f32 v223, v228, v2, v126
	s_cmp_ge_u32 s36, s12
	s_cbranch_scc1 .Lmla_exit_1
	v_mov_b32_e32 v227, v16
	s_waitcnt lgkmcnt(0)
	s_barrier
	ds_read_b128 v[4:7], v209 offset:40960
	ds_read_b128 v[8:11], v209 offset:45056
	ds_read_b128 v[174:177], v210 offset:40960
	ds_read_b128 v[246:249], v210 offset:45056
	ds_read_b128 v[250:253], v211 offset:40960
	ds_read_b128 v[78:81], v211 offset:45056
	ds_read_b128 v[12:15], v212 offset:40960
	v_exp_f32_e32 v98, v98
	v_exp_f32_e32 v99, v99
	v_exp_f32_e32 v100, v100
	v_exp_f32_e32 v101, v101
	v_exp_f32_e32 v102, v102
	v_exp_f32_e32 v103, v103
	v_exp_f32_e32 v104, v104
	v_exp_f32_e32 v105, v105
	s_waitcnt lgkmcnt(6)
	v_mfma_f32_32x32x16_bf16 v[130:145], v[4:7], v[166:169], v[82:97]
	ds_read_b128 v[4:7], v212 offset:45056
	v_exp_f32_e32 v106, v106
	v_exp_f32_e32 v107, v107
	v_exp_f32_e32 v108, v108
	v_cvt_pk_bf16_f32 v74, v243, v245
	s_waitcnt lgkmcnt(6)
	v_mfma_f32_32x32x16_bf16 v[114:129], v[8:11], v[166:169], v[82:97]
	ds_read_b128 v[8:11], v219 offset:49152
	v_exp_f32_e32 v109, v109
	v_exp_f32_e32 v110, v110
	v_exp_f32_e32 v111, v111
	v_cvt_pk_bf16_f32 v75, v241, v244
	s_waitcnt lgkmcnt(6)
	v_mfma_f32_32x32x16_bf16 v[130:145], v[174:177], v[162:165], v[130:145]
	ds_read_b128 v[174:177], v219 offset:51200
	v_exp_f32_e32 v112, v112
	v_exp_f32_e32 v113, v113
	v_cvt_pk_bf16_f32 v76, v239, v242
	v_cvt_pk_bf16_f32 v77, v238, v240
	v_add_f32_e32 v229, v243, v245
	v_add_f32_e32 v229, v241, v229
	s_waitcnt lgkmcnt(6)
	v_mfma_f32_32x32x16_bf16 v[114:129], v[246:249], v[162:165], v[114:129]
	ds_read_b128 v[246:249], v220 offset:49152
	v_cvt_pk_bf16_f32 v66, v236, v237
	v_cvt_pk_bf16_f32 v67, v233, v235
	v_add_f32_e32 v229, v244, v229
	v_add_f32_e32 v229, v239, v229
	v_add_f32_e32 v229, v242, v229
	v_add_f32_e32 v229, v238, v229
	s_waitcnt lgkmcnt(6)
	v_mfma_f32_32x32x16_bf16 v[130:145], v[250:253], v[158:161], v[130:145]
	ds_read_b128 v[250:253], v220 offset:51200
	v_cvt_pk_bf16_f32 v68, v231, v234
	v_cvt_pk_bf16_f32 v69, v230, v232
	v_add_f32_e32 v229, v240, v229
	v_add_f32_e32 v229, v236, v229
	v_add_f32_e32 v229, v237, v229
	v_add_f32_e32 v229, v233, v229
	s_waitcnt lgkmcnt(6)
	v_mfma_f32_32x32x16_bf16 v[114:129], v[78:81], v[158:161], v[114:129]
	v_add_f32_e32 v229, v235, v229
	v_add_f32_e32 v229, v231, v229
	v_add_f32_e32 v229, v234, v229
	v_add_f32_e32 v229, v230, v229
	v_add_f32_e32 v229, v232, v229
	v_add_f32_e32 v229, v98, v229
	s_waitcnt lgkmcnt(5)
	v_mfma_f32_32x32x16_bf16 v[130:145], v[12:15], v[154:157], v[130:145]
	ds_read_b64_tr_b16 v[230:231], v213 offset:20480
	ds_read_b64_tr_b16 v[232:233], v213 offset:21504
	ds_read_b64_tr_b16 v[234:235], v213 offset:22528
	ds_read_b64_tr_b16 v[236:237], v213 offset:23552
	v_add_f32_e32 v229, v99, v229
	v_add_f32_e32 v229, v100, v229
	v_add_f32_e32 v229, v101, v229
	s_waitcnt lgkmcnt(8)
	v_mfma_f32_32x32x16_bf16 v[114:129], v[4:7], v[154:157], v[114:129]
	ds_read_b64_tr_b16 v[238:239], v213 offset:24576
	ds_read_b64_tr_b16 v[240:241], v213 offset:25600
	ds_read_b64_tr_b16 v[242:243], v213 offset:26624
	ds_read_b64_tr_b16 v[244:245], v213 offset:27648
	v_add_f32_e32 v229, v102, v229
	v_add_f32_e32 v229, v103, v229
	v_add_f32_e32 v229, v104, v229
	s_waitcnt lgkmcnt(11)
	v_mfma_f32_32x32x16_bf16 v[130:145], v[8:11], v[150:153], v[130:145]
	v_add_f32_e32 v229, v105, v229
	v_add_f32_e32 v229, v106, v229
	v_add_f32_e32 v229, v107, v229
	v_add_f32_e32 v229, v108, v229
	v_add_f32_e32 v229, v109, v229
	v_add_f32_e32 v229, v110, v229
	s_waitcnt lgkmcnt(10)
	v_mfma_f32_32x32x16_bf16 v[114:129], v[174:177], v[150:153], v[114:129]
	v_add_f32_e32 v229, v111, v229
	v_add_f32_e32 v229, v112, v229
	v_add_f32_e32 v228, v113, v229
	s_add_i32 s36, s35, -1
	s_cmp_lt_u32 s36, s30
	s_cselect_b32 s0, 0, s30
	s_cselect_b32 s1, s29, s34
	s_lshl_b32 s0, s0, 6
	s_sub_i32 s37, s1, s0
	s_lshl_b32 s1, s36, 6
	s_add_i32 s37, s37, s1
	s_lshl_b32 s0, s37, 6
	s_add_u32 s48, s44, s0
	s_addc_u32 s49, s45, 0
	s_lshl_b32 s0, s37, 11
	s_add_u32 s46, s42, s0
	s_addc_u32 s47, s43, 0
	global_load_dwordx4 v[174:177], v226, s[48:49]
	s_waitcnt lgkmcnt(9)
	v_mfma_f32_32x32x16_bf16 v[130:145], v[246:249], v[146:149], v[130:145]
	v_cvt_pk_bf16_f32 v70, v98, v99
	v_cvt_pk_bf16_f32 v71, v100, v101
	v_cvt_pk_bf16_f32 v72, v102, v103
	v_cvt_pk_bf16_f32 v73, v104, v105
	global_load_dwordx4 v[8:11], v225, s[46:47]
	global_load_dwordx4 v[4:7], v225, s[46:47] offset:128
	s_waitcnt lgkmcnt(8)
	v_mfma_f32_32x32x16_bf16 v[114:129], v[250:253], v[146:149], v[114:129]
	v_cvt_pk_bf16_f32 v12, v106, v107
	v_cvt_pk_bf16_f32 v13, v108, v109
	v_cvt_pk_bf16_f32 v14, v110, v111
	v_cvt_pk_bf16_f32 v15, v112, v113
	ds_read_b64_tr_b16 v[78:79], v213 offset:20992
	ds_read_b64_tr_b16 v[80:81], v213 offset:22016
	ds_read_b64_tr_b16 v[98:99], v213 offset:23040
	ds_read_b64_tr_b16 v[100:101], v213 offset:24064
	ds_read_b64_tr_b16 v[102:103], v213 offset:25088
	ds_read_b64_tr_b16 v[104:105], v213 offset:26112
	ds_read_b64_tr_b16 v[110:111], v213 offset:27136
	ds_read_b64_tr_b16 v[112:113], v213 offset:28160
	v_max3_f32 v2, v130, v131, v132
	v_max3_f32 v2, v2, v133, v134
	v_max3_f32 v2, v2, v135, v136
	v_max3_f32 v2, v2, v137, v138
	v_max3_f32 v2, v2, v139, v140
	v_max3_f32 v2, v2, v141, v142
	s_waitcnt lgkmcnt(8)
	v_mfma_f32_32x32x16_bf16 v[50:65], v[230:233], v[74:77], v[50:65]
	v_max3_f32 v2, v2, v143, v144
	v_max3_f32 v2, v2, v145, v114
	v_max3_f32 v2, v2, v115, v116
	v_max3_f32 v2, v2, v117, v118
	v_mfma_f32_32x32x16_bf16 v[50:65], v[234:237], v[66:69], v[50:65]
	v_max3_f32 v2, v2, v119, v120
	v_max3_f32 v2, v2, v121, v122
	v_max3_f32 v2, v2, v123, v124
	v_mfma_f32_32x32x16_bf16 v[50:65], v[238:241], v[70:73], v[50:65]
	v_max3_f32 v2, v2, v125, v126
	v_max3_f32 v2, v2, v127, v128
	v_max_f32_e32 v2, v2, v129
	v_mfma_f32_32x32x16_bf16 v[50:65], v[242:245], v[12:15], v[50:65]
	v_cmp_ge_f32_e32 vcc, s28, v2
	s_cmp_eq_u64 vcc, exec
	s_cbranch_scc0 .LBB0_542_2
	v_mov_b32_e32 v2, 1.0

; #define SBAR() __builtin_amdgcn_sched_barrier(0)
; __device__ __forceinline__ float psm_max(const f32x16& p0, const f32x16& p1) {
;     float pmax = p0[0];
; #pragma unroll
;     for (int r = 1; r < 16; ++r) pmax = fmaxf(pmax, p0[r]);
; #pragma unroll
;     for (int r = 0; r < 16; ++r) pmax = fmaxf(pmax, p1[r]);
;     { auto rr = __builtin_amdgcn_permlane32_swap(__float_as_uint(pmax), __float_as_uint(pmax), false, false);
;       pmax = fmaxf(__uint_as_float(rr[0]), __uint_as_float(rr[1])); }
;     return pmax;
; }
; template <int D0> __device__ __forceinline__ void pv_one(f32x16& od, unsigned vb, bf16x8 pa0, bf16x8 pa1, bf16x8 pa2, bf16x8 pa3) {
;     const s16x4 l0 = tr_read<v_rd_off(D0, 0, 0)>(vb), h0 = tr_read<v_rd_off(D0, 0, 1)>(vb), l1 = tr_read<v_rd_off(D0, 1, 0)>(vb), h1 = tr_read<v_rd_off(D0, 1, 1)>(vb);
;     const s16x4 l2 = tr_read<v_rd_off(D0, 2, 0)>(vb), h2 = tr_read<v_rd_off(D0, 2, 1)>(vb), l3 = tr_read<v_rd_off(D0, 3, 0)>(vb), h3 = tr_read<v_rd_off(D0, 3, 1)>(vb);
;     asm volatile("s_waitcnt lgkmcnt(0)" ::: "memory"); SBAR();
;     ...
;     od = __builtin_amdgcn_mfma_f32_32x32x16_bf16(ATT_PK(l0, h0), pa0, od, 0, 0, 0);
;     od = __builtin_amdgcn_mfma_f32_32x32x16_bf16(ATT_PK(l1, h1), pa1, od, 0, 0, 0);
;     od = __builtin_amdgcn_mfma_f32_32x32x16_bf16(ATT_PK(l2, h2), pa2, od, 0, 0, 0);
;     od = __builtin_amdgcn_mfma_f32_32x32x16_bf16(ATT_PK(l3, h3), pa3, od, 0, 0, 0);
;     ...
; }
.Lmla_b_ld_done_2:
	s_waitcnt lgkmcnt(8)
	v_mfma_f32_32x32x16_bf16 v[98:113], v[70:73], v[146:149], v[98:113]
	v_cvt_pk_bf16_f32 v118, v122, v123
	v_cvt_pk_bf16_f32 v119, v124, v125
	v_cvt_pk_bf16_f32 v120, v126, v127
	v_cvt_pk_bf16_f32 v121, v128, v129
	v_add_f32_e32 v126, v129, v252
	ds_read_b64_tr_b16 v[66:67], v213 offset:41472
	ds_read_b64_tr_b16 v[68:69], v213 offset:42496
	ds_read_b64_tr_b16 v[70:71], v213 offset:43520
	ds_read_b64_tr_b16 v[72:73], v213 offset:44544
	ds_read_b64_tr_b16 v[74:75], v213 offset:45568
	ds_read_b64_tr_b16 v[76:77], v213 offset:46592
	ds_read_b64_tr_b16 v[78:79], v213 offset:47616
	ds_read_b64_tr_b16 v[80:81], v213 offset:48640
	v_max3_f32 v250, v130, v131, v132
	v_max3_f32 v250, v250, v133, v134
	v_max3_f32 v250, v250, v135, v136
	v_max3_f32 v250, v250, v137, v138
	v_max3_f32 v250, v250, v139, v140
	v_max3_f32 v250, v250, v141, v142
	s_waitcnt lgkmcnt(8)
	v_mfma_f32_32x32x16_bf16 v[50:65], v[234:237], v[12:15], v[50:65]
	v_max3_f32 v250, v250, v143, v144
	v_max3_f32 v250, v250, v145, v98
	v_max3_f32 v250, v250, v99, v100
	v_max3_f32 v250, v250, v101, v102
	v_mfma_f32_32x32x16_bf16 v[50:65], v[238:241], v[230:233], v[50:65]
	v_max3_f32 v250, v250, v103, v104
	v_max3_f32 v250, v250, v105, v106
	v_max3_f32 v250, v250, v107, v108
	v_mfma_f32_32x32x16_bf16 v[50:65], v[242:245], v[114:117], v[50:65]
	v_max3_f32 v250, v250, v109, v110
	v_max3_f32 v250, v250, v111, v112
	v_max_f32_e32 v250, v250, v113
	v_mfma_f32_32x32x16_bf16 v[50:65], v[246:249], v[118:121], v[50:65]
	v_cmp_ge_f32_e32 vcc, s28, v250
	s_cmp_eq_u64 vcc, exec
	v_mov_b32_e32 v16, 1.0
	s_cbranch_scc0 .LBB0_543_2
